# gather main loop rewritten by hand: 8 experts per iteration, next-group rows prefetched one iteration ahead via SGPR-base loads, transposing permlane/DPP reduction of 8 dots, one GELU per 8 experts
# speedup vs baseline: 1.1641x; 1.0117x over previous
.LBB0_1405:
	s_barrier
	s_ashr_i32 s45, s44, 31
	s_lshl_b64 s[0:1], s[44:45], 9
	v_lshl_or_b32 v0, v80, 2, s0
	v_mov_b32_e32 v1, s1
	v_lshl_add_u64 v[2:3], s[46:47], 0, v[0:1]
	v_or_b32_e32 v4, 0x100, v0
	v_mov_b32_e32 v5, s1
	v_lshl_add_u64 v[6:7], s[46:47], 0, v[4:5]
	v_lshl_add_u64 v[0:1], s[48:49], 0, v[0:1]
	v_lshl_add_u64 v[4:5], s[48:49], 0, v[4:5]
	global_load_dword v18, v[2:3], off
	global_load_dword v16, v[6:7], off
	global_load_dword v19, v[0:1], off
	global_load_dword v17, v[4:5], off
	s_lshl_b64 s[0:1], s[44:45], 12
	v_lshl_add_u64 v[100:101], v[84:85], 0, s[0:1]
	global_load_dwordx4 v[0:3], v[100:101], off offset:48
	global_load_dwordx4 v[4:7], v[100:101], off offset:32
	global_load_dwordx4 v[8:11], v[100:101], off offset:16
	global_load_dwordx4 v[12:15], v[100:101], off
	s_waitcnt vmcnt(4)
	v_lshrrev_b32_e32 v20, 10, v18
	v_lshrrev_b32_e32 v21, 10, v16
	v_mov_b32_e32 v24, 0
	v_cmp_eq_u32_e64 s[8:9], v20, 0
	v_cmp_eq_u32_e64 s[14:15], v21, 0
	s_bcnt1_i32_b64 s2, s[8:9]
	s_bcnt1_i32_b64 s4, s[14:15]
	v_mbcnt_lo_u32_b32 v25, s8, v24
	v_mbcnt_hi_u32_b32 v25, s9, v25
	v_add_u32_e32 v24, s2, v24
	v_cndmask_b32_e64 v22, v22, v25, s[8:9]
	v_mbcnt_lo_u32_b32 v26, s14, v24
	v_mbcnt_hi_u32_b32 v26, s15, v26
	v_add_u32_e32 v24, s4, v24
	v_cndmask_b32_e64 v23, v23, v26, s[14:15]
	v_cmp_eq_u32_e64 s[8:9], v20, 1
	v_cmp_eq_u32_e64 s[14:15], v21, 1
	s_bcnt1_i32_b64 s2, s[8:9]
	s_bcnt1_i32_b64 s4, s[14:15]
	v_mbcnt_lo_u32_b32 v25, s8, v24
	v_mbcnt_hi_u32_b32 v25, s9, v25
	v_add_u32_e32 v24, s2, v24
	v_cndmask_b32_e64 v22, v22, v25, s[8:9]
	v_mbcnt_lo_u32_b32 v26, s14, v24
	v_mbcnt_hi_u32_b32 v26, s15, v26
	v_add_u32_e32 v24, s4, v24
	v_cndmask_b32_e64 v23, v23, v26, s[14:15]
	v_cmp_eq_u32_e64 s[8:9], v20, 2
	v_cmp_eq_u32_e64 s[14:15], v21, 2
	s_bcnt1_i32_b64 s2, s[8:9]
	s_bcnt1_i32_b64 s4, s[14:15]
	v_mbcnt_lo_u32_b32 v25, s8, v24
	v_mbcnt_hi_u32_b32 v25, s9, v25
	v_add_u32_e32 v24, s2, v24
	v_cndmask_b32_e64 v22, v22, v25, s[8:9]
	v_mbcnt_lo_u32_b32 v26, s14, v24
	v_mbcnt_hi_u32_b32 v26, s15, v26
	v_add_u32_e32 v24, s4, v24
	v_cndmask_b32_e64 v23, v23, v26, s[14:15]
	v_cmp_eq_u32_e64 s[8:9], v20, 3
	v_cmp_eq_u32_e64 s[14:15], v21, 3
	s_bcnt1_i32_b64 s2, s[8:9]
	s_bcnt1_i32_b64 s4, s[14:15]
	v_mbcnt_lo_u32_b32 v25, s8, v24
	v_mbcnt_hi_u32_b32 v25, s9, v25
	v_add_u32_e32 v24, s2, v24
	v_cndmask_b32_e64 v22, v22, v25, s[8:9]
	v_mbcnt_lo_u32_b32 v26, s14, v24
	v_mbcnt_hi_u32_b32 v26, s15, v26
	v_add_u32_e32 v24, s4, v24
	v_cndmask_b32_e64 v23, v23, v26, s[14:15]
	v_cmp_eq_u32_e64 s[8:9], v20, 4
	v_cmp_eq_u32_e64 s[14:15], v21, 4
	s_bcnt1_i32_b64 s2, s[8:9]
	s_bcnt1_i32_b64 s4, s[14:15]
	v_mbcnt_lo_u32_b32 v25, s8, v24
	v_mbcnt_hi_u32_b32 v25, s9, v25
	v_add_u32_e32 v24, s2, v24
	v_cndmask_b32_e64 v22, v22, v25, s[8:9]
	v_mbcnt_lo_u32_b32 v26, s14, v24
	v_mbcnt_hi_u32_b32 v26, s15, v26
	v_add_u32_e32 v24, s4, v24
	v_cndmask_b32_e64 v23, v23, v26, s[14:15]
	v_cmp_eq_u32_e64 s[8:9], v20, 5
	v_cmp_eq_u32_e64 s[14:15], v21, 5
	s_bcnt1_i32_b64 s2, s[8:9]
	s_bcnt1_i32_b64 s4, s[14:15]
	v_mbcnt_lo_u32_b32 v25, s8, v24
	v_mbcnt_hi_u32_b32 v25, s9, v25
	v_add_u32_e32 v24, s2, v24
	v_cndmask_b32_e64 v22, v22, v25, s[8:9]
	v_mbcnt_lo_u32_b32 v26, s14, v24
	v_mbcnt_hi_u32_b32 v26, s15, v26
	v_add_u32_e32 v24, s4, v24
	v_cndmask_b32_e64 v23, v23, v26, s[14:15]
	v_cmp_eq_u32_e64 s[8:9], v20, 6
	v_cmp_eq_u32_e64 s[14:15], v21, 6
	s_bcnt1_i32_b64 s2, s[8:9]
	s_bcnt1_i32_b64 s4, s[14:15]
	v_mbcnt_lo_u32_b32 v25, s8, v24
	v_mbcnt_hi_u32_b32 v25, s9, v25
	v_add_u32_e32 v24, s2, v24
	v_cndmask_b32_e64 v22, v22, v25, s[8:9]
	v_mbcnt_lo_u32_b32 v26, s14, v24
	v_mbcnt_hi_u32_b32 v26, s15, v26
	v_add_u32_e32 v24, s4, v24
	v_cndmask_b32_e64 v23, v23, v26, s[14:15]
	v_cmp_eq_u32_e64 s[8:9], v20, 7
	v_cmp_eq_u32_e64 s[14:15], v21, 7
	s_bcnt1_i32_b64 s2, s[8:9]
	s_bcnt1_i32_b64 s4, s[14:15]
	v_mbcnt_lo_u32_b32 v25, s8, v24
	v_mbcnt_hi_u32_b32 v25, s9, v25
	v_add_u32_e32 v24, s2, v24
	v_cndmask_b32_e64 v22, v22, v25, s[8:9]
	v_mbcnt_lo_u32_b32 v26, s14, v24
	v_mbcnt_hi_u32_b32 v26, s15, v26
	v_add_u32_e32 v24, s4, v24
	v_cndmask_b32_e64 v23, v23, v26, s[14:15]
	v_cmp_eq_u32_e64 s[8:9], v20, 8
	v_cmp_eq_u32_e64 s[14:15], v21, 8
	s_bcnt1_i32_b64 s2, s[8:9]
	s_bcnt1_i32_b64 s4, s[14:15]
	v_mbcnt_lo_u32_b32 v25, s8, v24
	v_mbcnt_hi_u32_b32 v25, s9, v25
	v_add_u32_e32 v24, s2, v24
	v_cndmask_b32_e64 v22, v22, v25, s[8:9]
	v_mbcnt_lo_u32_b32 v26, s14, v24
	v_mbcnt_hi_u32_b32 v26, s15, v26
	v_add_u32_e32 v24, s4, v24
	v_cndmask_b32_e64 v23, v23, v26, s[14:15]
	v_cmp_eq_u32_e64 s[8:9], v20, 9
	v_cmp_eq_u32_e64 s[14:15], v21, 9
	s_bcnt1_i32_b64 s2, s[8:9]
	s_bcnt1_i32_b64 s4, s[14:15]
	v_mbcnt_lo_u32_b32 v25, s8, v24
	v_mbcnt_hi_u32_b32 v25, s9, v25
	v_add_u32_e32 v24, s2, v24
	v_cndmask_b32_e64 v22, v22, v25, s[8:9]
	v_mbcnt_lo_u32_b32 v26, s14, v24
	v_mbcnt_hi_u32_b32 v26, s15, v26
	v_add_u32_e32 v24, s4, v24
	v_cndmask_b32_e64 v23, v23, v26, s[14:15]
	v_cmp_eq_u32_e64 s[8:9], v20, 10
	v_cmp_eq_u32_e64 s[14:15], v21, 10
	s_bcnt1_i32_b64 s2, s[8:9]
	s_bcnt1_i32_b64 s4, s[14:15]
	v_mbcnt_lo_u32_b32 v25, s8, v24
	v_mbcnt_hi_u32_b32 v25, s9, v25
	v_add_u32_e32 v24, s2, v24
	v_cndmask_b32_e64 v22, v22, v25, s[8:9]
	v_mbcnt_lo_u32_b32 v26, s14, v24
	v_mbcnt_hi_u32_b32 v26, s15, v26
	v_add_u32_e32 v24, s4, v24
	v_cndmask_b32_e64 v23, v23, v26, s[14:15]
	v_cmp_eq_u32_e64 s[8:9], v20, 11
	v_cmp_eq_u32_e64 s[14:15], v21, 11
	s_bcnt1_i32_b64 s2, s[8:9]
	s_bcnt1_i32_b64 s4, s[14:15]
	v_mbcnt_lo_u32_b32 v25, s8, v24
	v_mbcnt_hi_u32_b32 v25, s9, v25
	v_add_u32_e32 v24, s2, v24
	v_cndmask_b32_e64 v22, v22, v25, s[8:9]
	v_mbcnt_lo_u32_b32 v26, s14, v24
	v_mbcnt_hi_u32_b32 v26, s15, v26
	v_add_u32_e32 v24, s4, v24
	v_cndmask_b32_e64 v23, v23, v26, s[14:15]
	v_cmp_eq_u32_e64 s[8:9], v20, 12
	v_cmp_eq_u32_e64 s[14:15], v21, 12
	s_bcnt1_i32_b64 s2, s[8:9]
	s_bcnt1_i32_b64 s4, s[14:15]
	v_mbcnt_lo_u32_b32 v25, s8, v24
	v_mbcnt_hi_u32_b32 v25, s9, v25
	v_add_u32_e32 v24, s2, v24
	v_cndmask_b32_e64 v22, v22, v25, s[8:9]
	v_mbcnt_lo_u32_b32 v26, s14, v24
	v_mbcnt_hi_u32_b32 v26, s15, v26
	v_add_u32_e32 v24, s4, v24
	v_cndmask_b32_e64 v23, v23, v26, s[14:15]
	v_cmp_eq_u32_e64 s[8:9], v20, 13
	v_cmp_eq_u32_e64 s[14:15], v21, 13
	s_bcnt1_i32_b64 s2, s[8:9]
	s_bcnt1_i32_b64 s4, s[14:15]
	v_mbcnt_lo_u32_b32 v25, s8, v24
	v_mbcnt_hi_u32_b32 v25, s9, v25
	v_add_u32_e32 v24, s2, v24
	v_cndmask_b32_e64 v22, v22, v25, s[8:9]
	v_mbcnt_lo_u32_b32 v26, s14, v24
	v_mbcnt_hi_u32_b32 v26, s15, v26
	v_add_u32_e32 v24, s4, v24
	v_cndmask_b32_e64 v23, v23, v26, s[14:15]
	v_cmp_eq_u32_e64 s[8:9], v20, 14
	v_cmp_eq_u32_e64 s[14:15], v21, 14
	s_bcnt1_i32_b64 s2, s[8:9]
	s_bcnt1_i32_b64 s4, s[14:15]
	v_mbcnt_lo_u32_b32 v25, s8, v24
	v_mbcnt_hi_u32_b32 v25, s9, v25
	v_add_u32_e32 v24, s2, v24
	v_cndmask_b32_e64 v22, v22, v25, s[8:9]
	v_mbcnt_lo_u32_b32 v26, s14, v24
	v_mbcnt_hi_u32_b32 v26, s15, v26
	v_add_u32_e32 v24, s4, v24
	v_cndmask_b32_e64 v23, v23, v26, s[14:15]
	v_cmp_eq_u32_e64 s[8:9], v20, 15
	v_cmp_eq_u32_e64 s[14:15], v21, 15
	s_bcnt1_i32_b64 s2, s[8:9]
	s_bcnt1_i32_b64 s4, s[14:15]
	v_mbcnt_lo_u32_b32 v25, s8, v24
	v_mbcnt_hi_u32_b32 v25, s9, v25
	v_add_u32_e32 v24, s2, v24
	v_cndmask_b32_e64 v22, v22, v25, s[8:9]
	v_mbcnt_lo_u32_b32 v26, s14, v24
	v_mbcnt_hi_u32_b32 v26, s15, v26
	v_add_u32_e32 v24, s4, v24
	v_cndmask_b32_e64 v23, v23, v26, s[14:15]
	v_lshl_add_u32 v250, v22, 3, s21
	v_lshl_add_u32 v251, v23, 3, s21
	ds_write_b64 v250, v[18:19] offset:1024
	ds_write_b64 v251, v[16:17] offset:1024
	v_and_b32_e32 v212, 7, v80
	v_lshl_add_u32 v212, v212, 3, s21
	v_add_u32_e32 v212, 0x400, v212
	v_lshrrev_b32_e32 v213, 4, v80
	v_bfe_u32 v250, v80, 3, 1
	v_lshl_add_u32 v213, v213, 1, v250
	v_lshl_add_u32 v213, v213, 3, s21
	v_add_u32_e32 v213, 0x404, v213
	ds_read_b32 v200, v212
	s_waitcnt vmcnt(0)
	v_lshlrev_b32_e32 v102, 16, v12
	v_and_b32_e32 v103, 0xffff0000, v12
	v_lshlrev_b32_e32 v104, 16, v13
	v_and_b32_e32 v105, 0xffff0000, v13
	v_lshlrev_b32_e32 v106, 16, v14
	v_and_b32_e32 v107, 0xffff0000, v14
	v_lshlrev_b32_e32 v108, 16, v15
	v_and_b32_e32 v109, 0xffff0000, v15
	v_lshlrev_b32_e32 v110, 16, v8
	v_and_b32_e32 v111, 0xffff0000, v8
	v_lshlrev_b32_e32 v112, 16, v9
	v_and_b32_e32 v113, 0xffff0000, v9
	v_lshlrev_b32_e32 v114, 16, v10
	v_and_b32_e32 v115, 0xffff0000, v10
	v_lshlrev_b32_e32 v116, 16, v11
	v_and_b32_e32 v117, 0xffff0000, v11
	v_lshlrev_b32_e32 v118, 16, v4
	v_and_b32_e32 v119, 0xffff0000, v4
	v_lshlrev_b32_e32 v120, 16, v5
	v_and_b32_e32 v121, 0xffff0000, v5
	v_lshlrev_b32_e32 v122, 16, v6
	v_and_b32_e32 v123, 0xffff0000, v6
	v_lshlrev_b32_e32 v124, 16, v7
	v_and_b32_e32 v125, 0xffff0000, v7
	v_lshlrev_b32_e32 v126, 16, v0
	v_and_b32_e32 v127, 0xffff0000, v0
	v_lshlrev_b32_e32 v128, 16, v1
	v_and_b32_e32 v129, 0xffff0000, v1
	v_lshlrev_b32_e32 v130, 16, v2
	v_and_b32_e32 v131, 0xffff0000, v2
	v_lshlrev_b32_e32 v132, 16, v3
	v_and_b32_e32 v133, 0xffff0000, v3
	v_mov_b32_e32 v178, 0
	v_mov_b32_e32 v179, 0
	v_mov_b32_e32 v184, 0
	v_mov_b32_e32 v185, 0
	v_mov_b32_e32 v182, 0
	v_mov_b32_e32 v183, 0
	v_mov_b32_e32 v180, 0
	v_mov_b32_e32 v181, 0
	v_mov_b32_e32 v176, 0
	v_mov_b32_e32 v177, 0
	v_mov_b32_e32 v174, 0
	v_mov_b32_e32 v175, 0
	v_mov_b32_e32 v160, 0
	v_mov_b32_e32 v161, 0
	v_mov_b32_e32 v158, 0
	v_mov_b32_e32 v159, 0
	v_mov_b32_e32 v156, 0
	v_mov_b32_e32 v157, 0
	v_mov_b32_e32 v154, 0
	v_mov_b32_e32 v155, 0
	v_mov_b32_e32 v152, 0
	v_mov_b32_e32 v153, 0
	v_mov_b32_e32 v150, 0
	v_mov_b32_e32 v151, 0
	v_mov_b32_e32 v148, 0
	v_mov_b32_e32 v149, 0
	v_mov_b32_e32 v146, 0
	v_mov_b32_e32 v147, 0
	v_mov_b32_e32 v144, 0
	v_mov_b32_e32 v145, 0
	v_mov_b32_e32 v142, 0
	v_mov_b32_e32 v143, 0
	s_waitcnt lgkmcnt(0)
	v_readlane_b32 s74, v200, 0
	s_lshl_b32 s24, s74, 10
	v_readlane_b32 s74, v200, 1
	s_lshl_b32 s28, s74, 10
	v_readlane_b32 s74, v200, 2
	s_lshl_b32 s29, s74, 10
	v_readlane_b32 s74, v200, 3
	s_lshl_b32 s34, s74, 10
	v_readlane_b32 s74, v200, 4
	s_lshl_b32 s35, s74, 10
	v_readlane_b32 s74, v200, 5
	s_lshl_b32 s42, s74, 10
	v_readlane_b32 s74, v200, 6
	s_lshl_b32 s43, s74, 10
	v_readlane_b32 s74, v200, 7
	s_lshl_b32 s50, s74, 10
	s_add_u32 s0, s93, s24
	s_addc_u32 s1, s20, 0
	global_load_dwordx4 v[0:3], v81, s[0:1]
	s_add_u32 s4, s93, s28
	s_addc_u32 s5, s20, 0
	global_load_dwordx4 v[4:7], v81, s[4:5]
	s_add_u32 s0, s93, s29
	s_addc_u32 s1, s20, 0
	global_load_dwordx4 v[8:11], v81, s[0:1]
	s_add_u32 s4, s93, s34
	s_addc_u32 s5, s20, 0
	global_load_dwordx4 v[12:15], v81, s[4:5]
	s_add_u32 s0, s93, s35
	s_addc_u32 s1, s20, 0
	global_load_dwordx4 v[16:19], v81, s[0:1]
	s_add_u32 s4, s93, s42
	s_addc_u32 s5, s20, 0
	global_load_dwordx4 v[20:23], v81, s[4:5]
	s_add_u32 s0, s93, s43
	s_addc_u32 s1, s20, 0
	global_load_dwordx4 v[24:27], v81, s[0:1]
	s_add_u32 s4, s93, s50
	s_addc_u32 s5, s20, 0
	global_load_dwordx4 v[28:31], v81, s[4:5]
	s_add_u32 s0, s89, s24
	s_addc_u32 s1, s92, 0
	global_load_dwordx4 v[36:39], v81, s[0:1]
	s_add_u32 s4, s89, s28
	s_addc_u32 s5, s92, 0
	global_load_dwordx4 v[40:43], v81, s[4:5]
	s_lshr_b32 s8, s24, 6
	s_add_u32 s8, s6, s8
	s_addc_u32 s9, s88, 0
	global_load_dword v68, v83, s[8:9]
	s_lshr_b32 s14, s28, 6
	s_add_u32 s14, s6, s14
	s_addc_u32 s15, s88, 0
	global_load_dword v69, v83, s[14:15]
	s_add_u32 s0, s89, s29
	s_addc_u32 s1, s92, 0
	global_load_dwordx4 v[44:47], v81, s[0:1]
	s_add_u32 s4, s89, s34
	s_addc_u32 s5, s92, 0
	global_load_dwordx4 v[48:51], v81, s[4:5]
	s_lshr_b32 s8, s29, 6
	s_add_u32 s8, s6, s8
	s_addc_u32 s9, s88, 0
	global_load_dword v70, v83, s[8:9]
	s_lshr_b32 s14, s34, 6
	s_add_u32 s14, s6, s14
	s_addc_u32 s15, s88, 0
	global_load_dword v71, v83, s[14:15]
	s_add_u32 s0, s89, s35
	s_addc_u32 s1, s92, 0
	global_load_dwordx4 v[52:55], v81, s[0:1]
	s_add_u32 s4, s89, s42
	s_addc_u32 s5, s92, 0
	global_load_dwordx4 v[56:59], v81, s[4:5]
	s_lshr_b32 s8, s35, 6
	s_add_u32 s8, s6, s8
	s_addc_u32 s9, s88, 0
	global_load_dword v72, v83, s[8:9]
	s_lshr_b32 s14, s42, 6
	s_add_u32 s14, s6, s14
	s_addc_u32 s15, s88, 0
	global_load_dword v73, v83, s[14:15]
	s_add_u32 s0, s89, s43
	s_addc_u32 s1, s92, 0
	global_load_dwordx4 v[60:63], v81, s[0:1]
	s_add_u32 s4, s89, s50
	s_addc_u32 s5, s92, 0
	global_load_dwordx4 v[64:67], v81, s[4:5]
	s_lshr_b32 s8, s43, 6
	s_add_u32 s8, s6, s8
	s_addc_u32 s9, s88, 0
	global_load_dword v74, v83, s[8:9]
	s_lshr_b32 s14, s50, 6
	s_add_u32 s14, s6, s14
	s_addc_u32 s15, s88, 0
	global_load_dword v75, v83, s[14:15]
	s_mov_b32 s2, 0
.Lgm_loop:
	s_add_i32 s0, s2, 64
	s_min_u32 s0, s0, 0x3c0
	v_add_u32_e32 v250, s0, v212
	v_add_u32_e32 v251, s2, v213
	ds_read_b32 v200, v250
	ds_read_b32 v201, v251
	s_waitcnt vmcnt(22)
	v_cvt_scalef32_pk_f32_fp4 v[228:229], v0, 1.0
	v_cvt_scalef32_pk_f32_fp4 v[230:231], v0, 1.0 op_sel:[1,0,0]
	v_cvt_scalef32_pk_f32_fp4 v[232:233], v0, 1.0 op_sel:[0,1,0]
	v_cvt_scalef32_pk_f32_fp4 v[234:235], v0, 1.0 op_sel:[1,1,0]
	v_cvt_scalef32_pk_f32_fp4 v[236:237], v4, 1.0
	v_cvt_scalef32_pk_f32_fp4 v[238:239], v4, 1.0 op_sel:[1,0,0]
	v_cvt_scalef32_pk_f32_fp4 v[240:241], v4, 1.0 op_sel:[0,1,0]
	v_cvt_scalef32_pk_f32_fp4 v[242:243], v4, 1.0 op_sel:[1,1,0]
	v_pk_mul_f32 v[244:245], v[228:229], v[102:103]
	v_pk_mul_f32 v[246:247], v[236:237], v[102:103]
	v_pk_fma_f32 v[244:245], v[230:231], v[104:105], v[244:245]
	v_pk_fma_f32 v[246:247], v[238:239], v[104:105], v[246:247]
	v_pk_fma_f32 v[244:245], v[232:233], v[106:107], v[244:245]
	v_pk_fma_f32 v[246:247], v[240:241], v[106:107], v[246:247]
	v_pk_fma_f32 v[244:245], v[234:235], v[108:109], v[244:245]
	v_pk_fma_f32 v[246:247], v[242:243], v[108:109], v[246:247]
	v_cvt_scalef32_pk_f32_fp4 v[228:229], v1, 1.0
	v_cvt_scalef32_pk_f32_fp4 v[230:231], v1, 1.0 op_sel:[1,0,0]
	v_cvt_scalef32_pk_f32_fp4 v[232:233], v1, 1.0 op_sel:[0,1,0]
	v_cvt_scalef32_pk_f32_fp4 v[234:235], v1, 1.0 op_sel:[1,1,0]
	v_cvt_scalef32_pk_f32_fp4 v[236:237], v5, 1.0
	v_cvt_scalef32_pk_f32_fp4 v[238:239], v5, 1.0 op_sel:[1,0,0]
	v_cvt_scalef32_pk_f32_fp4 v[240:241], v5, 1.0 op_sel:[0,1,0]
	v_cvt_scalef32_pk_f32_fp4 v[242:243], v5, 1.0 op_sel:[1,1,0]
	v_pk_fma_f32 v[244:245], v[228:229], v[110:111], v[244:245]
	v_pk_fma_f32 v[246:247], v[236:237], v[110:111], v[246:247]
	v_pk_fma_f32 v[244:245], v[230:231], v[112:113], v[244:245]
	v_pk_fma_f32 v[246:247], v[238:239], v[112:113], v[246:247]
	v_pk_fma_f32 v[244:245], v[232:233], v[114:115], v[244:245]
	v_pk_fma_f32 v[246:247], v[240:241], v[114:115], v[246:247]
	v_pk_fma_f32 v[244:245], v[234:235], v[116:117], v[244:245]
	v_pk_fma_f32 v[246:247], v[242:243], v[116:117], v[246:247]
	v_cvt_scalef32_pk_f32_fp4 v[228:229], v2, 1.0
	v_cvt_scalef32_pk_f32_fp4 v[230:231], v2, 1.0 op_sel:[1,0,0]
	v_cvt_scalef32_pk_f32_fp4 v[232:233], v2, 1.0 op_sel:[0,1,0]
	v_cvt_scalef32_pk_f32_fp4 v[234:235], v2, 1.0 op_sel:[1,1,0]
	v_cvt_scalef32_pk_f32_fp4 v[236:237], v6, 1.0
	v_cvt_scalef32_pk_f32_fp4 v[238:239], v6, 1.0 op_sel:[1,0,0]
	v_cvt_scalef32_pk_f32_fp4 v[240:241], v6, 1.0 op_sel:[0,1,0]
	v_cvt_scalef32_pk_f32_fp4 v[242:243], v6, 1.0 op_sel:[1,1,0]
	v_pk_fma_f32 v[244:245], v[228:229], v[118:119], v[244:245]
	v_pk_fma_f32 v[246:247], v[236:237], v[118:119], v[246:247]
	v_pk_fma_f32 v[244:245], v[230:231], v[120:121], v[244:245]
	v_pk_fma_f32 v[246:247], v[238:239], v[120:121], v[246:247]
	v_pk_fma_f32 v[244:245], v[232:233], v[122:123], v[244:245]
	v_pk_fma_f32 v[246:247], v[240:241], v[122:123], v[246:247]
	v_pk_fma_f32 v[244:245], v[234:235], v[124:125], v[244:245]
	v_pk_fma_f32 v[246:247], v[242:243], v[124:125], v[246:247]
	v_cvt_scalef32_pk_f32_fp4 v[228:229], v3, 1.0
	v_cvt_scalef32_pk_f32_fp4 v[230:231], v3, 1.0 op_sel:[1,0,0]
	v_cvt_scalef32_pk_f32_fp4 v[232:233], v3, 1.0 op_sel:[0,1,0]
	v_cvt_scalef32_pk_f32_fp4 v[234:235], v3, 1.0 op_sel:[1,1,0]
	v_cvt_scalef32_pk_f32_fp4 v[236:237], v7, 1.0
	v_cvt_scalef32_pk_f32_fp4 v[238:239], v7, 1.0 op_sel:[1,0,0]
	v_cvt_scalef32_pk_f32_fp4 v[240:241], v7, 1.0 op_sel:[0,1,0]
	v_cvt_scalef32_pk_f32_fp4 v[242:243], v7, 1.0 op_sel:[1,1,0]
	v_pk_fma_f32 v[244:245], v[228:229], v[126:127], v[244:245]
	v_pk_fma_f32 v[246:247], v[236:237], v[126:127], v[246:247]
	v_pk_fma_f32 v[244:245], v[230:231], v[128:129], v[244:245]
	v_pk_fma_f32 v[246:247], v[238:239], v[128:129], v[246:247]
	v_pk_fma_f32 v[244:245], v[232:233], v[130:131], v[244:245]
	v_pk_fma_f32 v[246:247], v[240:241], v[130:131], v[246:247]
	v_pk_fma_f32 v[244:245], v[234:235], v[132:133], v[244:245]
	v_pk_fma_f32 v[246:247], v[242:243], v[132:133], v[246:247]
	v_add_f32_e32 v186, v244, v245
	v_add_f32_e32 v187, v246, v247
	s_waitcnt lgkmcnt(0)
	v_readlane_b32 s74, v200, 0
	s_lshl_b32 s24, s74, 10
	v_readlane_b32 s74, v200, 1
	s_lshl_b32 s28, s74, 10
	v_readlane_b32 s74, v200, 2
	s_lshl_b32 s29, s74, 10
	v_readlane_b32 s74, v200, 3
	s_lshl_b32 s34, s74, 10
	v_readlane_b32 s74, v200, 4
	s_lshl_b32 s35, s74, 10
	v_readlane_b32 s74, v200, 5
	s_lshl_b32 s42, s74, 10
	v_readlane_b32 s74, v200, 6
	s_lshl_b32 s43, s74, 10
	v_readlane_b32 s74, v200, 7
	s_lshl_b32 s50, s74, 10
	s_add_u32 s0, s93, s24
	s_addc_u32 s1, s20, 0
	global_load_dwordx4 v[0:3], v81, s[0:1]
	s_add_u32 s4, s93, s28
	s_addc_u32 s5, s20, 0
	global_load_dwordx4 v[4:7], v81, s[4:5]
	s_waitcnt vmcnt(22)
	v_cvt_scalef32_pk_f32_fp4 v[228:229], v8, 1.0
	v_cvt_scalef32_pk_f32_fp4 v[230:231], v8, 1.0 op_sel:[1,0,0]
	v_cvt_scalef32_pk_f32_fp4 v[232:233], v8, 1.0 op_sel:[0,1,0]
	v_cvt_scalef32_pk_f32_fp4 v[234:235], v8, 1.0 op_sel:[1,1,0]
	v_cvt_scalef32_pk_f32_fp4 v[236:237], v12, 1.0
	v_cvt_scalef32_pk_f32_fp4 v[238:239], v12, 1.0 op_sel:[1,0,0]
	v_cvt_scalef32_pk_f32_fp4 v[240:241], v12, 1.0 op_sel:[0,1,0]
	v_cvt_scalef32_pk_f32_fp4 v[242:243], v12, 1.0 op_sel:[1,1,0]
	v_pk_mul_f32 v[244:245], v[228:229], v[102:103]
	v_pk_mul_f32 v[246:247], v[236:237], v[102:103]
	v_pk_fma_f32 v[244:245], v[230:231], v[104:105], v[244:245]
	v_pk_fma_f32 v[246:247], v[238:239], v[104:105], v[246:247]
	v_pk_fma_f32 v[244:245], v[232:233], v[106:107], v[244:245]
	v_pk_fma_f32 v[246:247], v[240:241], v[106:107], v[246:247]
	v_pk_fma_f32 v[244:245], v[234:235], v[108:109], v[244:245]
	v_pk_fma_f32 v[246:247], v[242:243], v[108:109], v[246:247]
	v_cvt_scalef32_pk_f32_fp4 v[228:229], v9, 1.0
	v_cvt_scalef32_pk_f32_fp4 v[230:231], v9, 1.0 op_sel:[1,0,0]
	v_cvt_scalef32_pk_f32_fp4 v[232:233], v9, 1.0 op_sel:[0,1,0]
	v_cvt_scalef32_pk_f32_fp4 v[234:235], v9, 1.0 op_sel:[1,1,0]
	v_cvt_scalef32_pk_f32_fp4 v[236:237], v13, 1.0
	v_cvt_scalef32_pk_f32_fp4 v[238:239], v13, 1.0 op_sel:[1,0,0]
	v_cvt_scalef32_pk_f32_fp4 v[240:241], v13, 1.0 op_sel:[0,1,0]
	v_cvt_scalef32_pk_f32_fp4 v[242:243], v13, 1.0 op_sel:[1,1,0]
	v_pk_fma_f32 v[244:245], v[228:229], v[110:111], v[244:245]
	v_pk_fma_f32 v[246:247], v[236:237], v[110:111], v[246:247]
	v_pk_fma_f32 v[244:245], v[230:231], v[112:113], v[244:245]
	v_pk_fma_f32 v[246:247], v[238:239], v[112:113], v[246:247]
	v_pk_fma_f32 v[244:245], v[232:233], v[114:115], v[244:245]
	v_pk_fma_f32 v[246:247], v[240:241], v[114:115], v[246:247]
	v_pk_fma_f32 v[244:245], v[234:235], v[116:117], v[244:245]
	v_pk_fma_f32 v[246:247], v[242:243], v[116:117], v[246:247]
	v_cvt_scalef32_pk_f32_fp4 v[228:229], v10, 1.0
	v_cvt_scalef32_pk_f32_fp4 v[230:231], v10, 1.0 op_sel:[1,0,0]
	v_cvt_scalef32_pk_f32_fp4 v[232:233], v10, 1.0 op_sel:[0,1,0]
	v_cvt_scalef32_pk_f32_fp4 v[234:235], v10, 1.0 op_sel:[1,1,0]
	v_cvt_scalef32_pk_f32_fp4 v[236:237], v14, 1.0
	v_cvt_scalef32_pk_f32_fp4 v[238:239], v14, 1.0 op_sel:[1,0,0]
	v_cvt_scalef32_pk_f32_fp4 v[240:241], v14, 1.0 op_sel:[0,1,0]
	v_cvt_scalef32_pk_f32_fp4 v[242:243], v14, 1.0 op_sel:[1,1,0]
	v_pk_fma_f32 v[244:245], v[228:229], v[118:119], v[244:245]
	v_pk_fma_f32 v[246:247], v[236:237], v[118:119], v[246:247]
	v_pk_fma_f32 v[244:245], v[230:231], v[120:121], v[244:245]
	v_pk_fma_f32 v[246:247], v[238:239], v[120:121], v[246:247]
	v_pk_fma_f32 v[244:245], v[232:233], v[122:123], v[244:245]
	v_pk_fma_f32 v[246:247], v[240:241], v[122:123], v[246:247]
	v_pk_fma_f32 v[244:245], v[234:235], v[124:125], v[244:245]
	v_pk_fma_f32 v[246:247], v[242:243], v[124:125], v[246:247]
	v_cvt_scalef32_pk_f32_fp4 v[228:229], v11, 1.0
	v_cvt_scalef32_pk_f32_fp4 v[230:231], v11, 1.0 op_sel:[1,0,0]
	v_cvt_scalef32_pk_f32_fp4 v[232:233], v11, 1.0 op_sel:[0,1,0]
	v_cvt_scalef32_pk_f32_fp4 v[234:235], v11, 1.0 op_sel:[1,1,0]
	v_cvt_scalef32_pk_f32_fp4 v[236:237], v15, 1.0
	v_cvt_scalef32_pk_f32_fp4 v[238:239], v15, 1.0 op_sel:[1,0,0]
	v_cvt_scalef32_pk_f32_fp4 v[240:241], v15, 1.0 op_sel:[0,1,0]
	v_cvt_scalef32_pk_f32_fp4 v[242:243], v15, 1.0 op_sel:[1,1,0]
	v_pk_fma_f32 v[244:245], v[228:229], v[126:127], v[244:245]
	v_pk_fma_f32 v[246:247], v[236:237], v[126:127], v[246:247]
	v_pk_fma_f32 v[244:245], v[230:231], v[128:129], v[244:245]
	v_pk_fma_f32 v[246:247], v[238:239], v[128:129], v[246:247]
	v_pk_fma_f32 v[244:245], v[232:233], v[130:131], v[244:245]
	v_pk_fma_f32 v[246:247], v[240:241], v[130:131], v[246:247]
	v_pk_fma_f32 v[244:245], v[234:235], v[132:133], v[244:245]
	v_pk_fma_f32 v[246:247], v[242:243], v[132:133], v[246:247]
	v_add_f32_e32 v188, v244, v245
	v_add_f32_e32 v189, v246, v247
	s_add_u32 s0, s93, s29
	s_addc_u32 s1, s20, 0
	global_load_dwordx4 v[8:11], v81, s[0:1]
	s_add_u32 s4, s93, s34
	s_addc_u32 s5, s20, 0
	global_load_dwordx4 v[12:15], v81, s[4:5]
	s_waitcnt vmcnt(22)
	v_cvt_scalef32_pk_f32_fp4 v[228:229], v16, 1.0
	v_cvt_scalef32_pk_f32_fp4 v[230:231], v16, 1.0 op_sel:[1,0,0]
	v_cvt_scalef32_pk_f32_fp4 v[232:233], v16, 1.0 op_sel:[0,1,0]
	v_cvt_scalef32_pk_f32_fp4 v[234:235], v16, 1.0 op_sel:[1,1,0]
	v_cvt_scalef32_pk_f32_fp4 v[236:237], v20, 1.0
	v_cvt_scalef32_pk_f32_fp4 v[238:239], v20, 1.0 op_sel:[1,0,0]
	v_cvt_scalef32_pk_f32_fp4 v[240:241], v20, 1.0 op_sel:[0,1,0]
	v_cvt_scalef32_pk_f32_fp4 v[242:243], v20, 1.0 op_sel:[1,1,0]
	v_pk_mul_f32 v[244:245], v[228:229], v[102:103]
	v_pk_mul_f32 v[246:247], v[236:237], v[102:103]
	v_pk_fma_f32 v[244:245], v[230:231], v[104:105], v[244:245]
	v_pk_fma_f32 v[246:247], v[238:239], v[104:105], v[246:247]
	v_pk_fma_f32 v[244:245], v[232:233], v[106:107], v[244:245]
	v_pk_fma_f32 v[246:247], v[240:241], v[106:107], v[246:247]
	v_pk_fma_f32 v[244:245], v[234:235], v[108:109], v[244:245]
	v_pk_fma_f32 v[246:247], v[242:243], v[108:109], v[246:247]
	v_cvt_scalef32_pk_f32_fp4 v[228:229], v17, 1.0
	v_cvt_scalef32_pk_f32_fp4 v[230:231], v17, 1.0 op_sel:[1,0,0]
	v_cvt_scalef32_pk_f32_fp4 v[232:233], v17, 1.0 op_sel:[0,1,0]
	v_cvt_scalef32_pk_f32_fp4 v[234:235], v17, 1.0 op_sel:[1,1,0]
	v_cvt_scalef32_pk_f32_fp4 v[236:237], v21, 1.0
	v_cvt_scalef32_pk_f32_fp4 v[238:239], v21, 1.0 op_sel:[1,0,0]
	v_cvt_scalef32_pk_f32_fp4 v[240:241], v21, 1.0 op_sel:[0,1,0]
	v_cvt_scalef32_pk_f32_fp4 v[242:243], v21, 1.0 op_sel:[1,1,0]
	v_pk_fma_f32 v[244:245], v[228:229], v[110:111], v[244:245]
	v_pk_fma_f32 v[246:247], v[236:237], v[110:111], v[246:247]
	v_pk_fma_f32 v[244:245], v[230:231], v[112:113], v[244:245]
	v_pk_fma_f32 v[246:247], v[238:239], v[112:113], v[246:247]
	v_pk_fma_f32 v[244:245], v[232:233], v[114:115], v[244:245]
	v_pk_fma_f32 v[246:247], v[240:241], v[114:115], v[246:247]
	v_pk_fma_f32 v[244:245], v[234:235], v[116:117], v[244:245]
	v_pk_fma_f32 v[246:247], v[242:243], v[116:117], v[246:247]
	v_cvt_scalef32_pk_f32_fp4 v[228:229], v18, 1.0
	v_cvt_scalef32_pk_f32_fp4 v[230:231], v18, 1.0 op_sel:[1,0,0]
	v_cvt_scalef32_pk_f32_fp4 v[232:233], v18, 1.0 op_sel:[0,1,0]
	v_cvt_scalef32_pk_f32_fp4 v[234:235], v18, 1.0 op_sel:[1,1,0]
	v_cvt_scalef32_pk_f32_fp4 v[236:237], v22, 1.0
	v_cvt_scalef32_pk_f32_fp4 v[238:239], v22, 1.0 op_sel:[1,0,0]
	v_cvt_scalef32_pk_f32_fp4 v[240:241], v22, 1.0 op_sel:[0,1,0]
	v_cvt_scalef32_pk_f32_fp4 v[242:243], v22, 1.0 op_sel:[1,1,0]
	v_pk_fma_f32 v[244:245], v[228:229], v[118:119], v[244:245]
	v_pk_fma_f32 v[246:247], v[236:237], v[118:119], v[246:247]
	v_pk_fma_f32 v[244:245], v[230:231], v[120:121], v[244:245]
	v_pk_fma_f32 v[246:247], v[238:239], v[120:121], v[246:247]
	v_pk_fma_f32 v[244:245], v[232:233], v[122:123], v[244:245]
	v_pk_fma_f32 v[246:247], v[240:241], v[122:123], v[246:247]
	v_pk_fma_f32 v[244:245], v[234:235], v[124:125], v[244:245]
	v_pk_fma_f32 v[246:247], v[242:243], v[124:125], v[246:247]
	v_cvt_scalef32_pk_f32_fp4 v[228:229], v19, 1.0
	v_cvt_scalef32_pk_f32_fp4 v[230:231], v19, 1.0 op_sel:[1,0,0]
	v_cvt_scalef32_pk_f32_fp4 v[232:233], v19, 1.0 op_sel:[0,1,0]
	v_cvt_scalef32_pk_f32_fp4 v[234:235], v19, 1.0 op_sel:[1,1,0]
	v_cvt_scalef32_pk_f32_fp4 v[236:237], v23, 1.0
	v_cvt_scalef32_pk_f32_fp4 v[238:239], v23, 1.0 op_sel:[1,0,0]
	v_cvt_scalef32_pk_f32_fp4 v[240:241], v23, 1.0 op_sel:[0,1,0]
	v_cvt_scalef32_pk_f32_fp4 v[242:243], v23, 1.0 op_sel:[1,1,0]
	v_pk_fma_f32 v[244:245], v[228:229], v[126:127], v[244:245]
	v_pk_fma_f32 v[246:247], v[236:237], v[126:127], v[246:247]
	v_pk_fma_f32 v[244:245], v[230:231], v[128:129], v[244:245]
	v_pk_fma_f32 v[246:247], v[238:239], v[128:129], v[246:247]
	v_pk_fma_f32 v[244:245], v[232:233], v[130:131], v[244:245]
	v_pk_fma_f32 v[246:247], v[240:241], v[130:131], v[246:247]
	v_pk_fma_f32 v[244:245], v[234:235], v[132:133], v[244:245]
	v_pk_fma_f32 v[246:247], v[242:243], v[132:133], v[246:247]
	v_add_f32_e32 v190, v244, v245
	v_add_f32_e32 v191, v246, v247
	s_add_u32 s0, s93, s35
	s_addc_u32 s1, s20, 0
	global_load_dwordx4 v[16:19], v81, s[0:1]
	s_add_u32 s4, s93, s42
	s_addc_u32 s5, s20, 0
	global_load_dwordx4 v[20:23], v81, s[4:5]
	s_waitcnt vmcnt(22)
	v_cvt_scalef32_pk_f32_fp4 v[228:229], v24, 1.0
	v_cvt_scalef32_pk_f32_fp4 v[230:231], v24, 1.0 op_sel:[1,0,0]
	v_cvt_scalef32_pk_f32_fp4 v[232:233], v24, 1.0 op_sel:[0,1,0]
	v_cvt_scalef32_pk_f32_fp4 v[234:235], v24, 1.0 op_sel:[1,1,0]
	v_cvt_scalef32_pk_f32_fp4 v[236:237], v28, 1.0
	v_cvt_scalef32_pk_f32_fp4 v[238:239], v28, 1.0 op_sel:[1,0,0]
	v_cvt_scalef32_pk_f32_fp4 v[240:241], v28, 1.0 op_sel:[0,1,0]
	v_cvt_scalef32_pk_f32_fp4 v[242:243], v28, 1.0 op_sel:[1,1,0]
	v_pk_mul_f32 v[244:245], v[228:229], v[102:103]
	v_pk_mul_f32 v[246:247], v[236:237], v[102:103]
	v_pk_fma_f32 v[244:245], v[230:231], v[104:105], v[244:245]
	v_pk_fma_f32 v[246:247], v[238:239], v[104:105], v[246:247]
	v_pk_fma_f32 v[244:245], v[232:233], v[106:107], v[244:245]
	v_pk_fma_f32 v[246:247], v[240:241], v[106:107], v[246:247]
	v_pk_fma_f32 v[244:245], v[234:235], v[108:109], v[244:245]
	v_pk_fma_f32 v[246:247], v[242:243], v[108:109], v[246:247]
	v_cvt_scalef32_pk_f32_fp4 v[228:229], v25, 1.0
	v_cvt_scalef32_pk_f32_fp4 v[230:231], v25, 1.0 op_sel:[1,0,0]
	v_cvt_scalef32_pk_f32_fp4 v[232:233], v25, 1.0 op_sel:[0,1,0]
	v_cvt_scalef32_pk_f32_fp4 v[234:235], v25, 1.0 op_sel:[1,1,0]
	v_cvt_scalef32_pk_f32_fp4 v[236:237], v29, 1.0
	v_cvt_scalef32_pk_f32_fp4 v[238:239], v29, 1.0 op_sel:[1,0,0]
	v_cvt_scalef32_pk_f32_fp4 v[240:241], v29, 1.0 op_sel:[0,1,0]
	v_cvt_scalef32_pk_f32_fp4 v[242:243], v29, 1.0 op_sel:[1,1,0]
	v_pk_fma_f32 v[244:245], v[228:229], v[110:111], v[244:245]
	v_pk_fma_f32 v[246:247], v[236:237], v[110:111], v[246:247]
	v_pk_fma_f32 v[244:245], v[230:231], v[112:113], v[244:245]
	v_pk_fma_f32 v[246:247], v[238:239], v[112:113], v[246:247]
	v_pk_fma_f32 v[244:245], v[232:233], v[114:115], v[244:245]
	v_pk_fma_f32 v[246:247], v[240:241], v[114:115], v[246:247]
	v_pk_fma_f32 v[244:245], v[234:235], v[116:117], v[244:245]
	v_pk_fma_f32 v[246:247], v[242:243], v[116:117], v[246:247]
	v_cvt_scalef32_pk_f32_fp4 v[228:229], v26, 1.0
	v_cvt_scalef32_pk_f32_fp4 v[230:231], v26, 1.0 op_sel:[1,0,0]
	v_cvt_scalef32_pk_f32_fp4 v[232:233], v26, 1.0 op_sel:[0,1,0]
	v_cvt_scalef32_pk_f32_fp4 v[234:235], v26, 1.0 op_sel:[1,1,0]
	v_cvt_scalef32_pk_f32_fp4 v[236:237], v30, 1.0
	v_cvt_scalef32_pk_f32_fp4 v[238:239], v30, 1.0 op_sel:[1,0,0]
	v_cvt_scalef32_pk_f32_fp4 v[240:241], v30, 1.0 op_sel:[0,1,0]
	v_cvt_scalef32_pk_f32_fp4 v[242:243], v30, 1.0 op_sel:[1,1,0]
	v_pk_fma_f32 v[244:245], v[228:229], v[118:119], v[244:245]
	v_pk_fma_f32 v[246:247], v[236:237], v[118:119], v[246:247]
	v_pk_fma_f32 v[244:245], v[230:231], v[120:121], v[244:245]
	v_pk_fma_f32 v[246:247], v[238:239], v[120:121], v[246:247]
	v_pk_fma_f32 v[244:245], v[232:233], v[122:123], v[244:245]
	v_pk_fma_f32 v[246:247], v[240:241], v[122:123], v[246:247]
	v_pk_fma_f32 v[244:245], v[234:235], v[124:125], v[244:245]
	v_pk_fma_f32 v[246:247], v[242:243], v[124:125], v[246:247]
	v_cvt_scalef32_pk_f32_fp4 v[228:229], v27, 1.0
	v_cvt_scalef32_pk_f32_fp4 v[230:231], v27, 1.0 op_sel:[1,0,0]
	v_cvt_scalef32_pk_f32_fp4 v[232:233], v27, 1.0 op_sel:[0,1,0]
	v_cvt_scalef32_pk_f32_fp4 v[234:235], v27, 1.0 op_sel:[1,1,0]
	v_cvt_scalef32_pk_f32_fp4 v[236:237], v31, 1.0
	v_cvt_scalef32_pk_f32_fp4 v[238:239], v31, 1.0 op_sel:[1,0,0]
	v_cvt_scalef32_pk_f32_fp4 v[240:241], v31, 1.0 op_sel:[0,1,0]
	v_cvt_scalef32_pk_f32_fp4 v[242:243], v31, 1.0 op_sel:[1,1,0]
	v_pk_fma_f32 v[244:245], v[228:229], v[126:127], v[244:245]
	v_pk_fma_f32 v[246:247], v[236:237], v[126:127], v[246:247]
	v_pk_fma_f32 v[244:245], v[230:231], v[128:129], v[244:245]
	v_pk_fma_f32 v[246:247], v[238:239], v[128:129], v[246:247]
	v_pk_fma_f32 v[244:245], v[232:233], v[130:131], v[244:245]
	v_pk_fma_f32 v[246:247], v[240:241], v[130:131], v[246:247]
	v_pk_fma_f32 v[244:245], v[234:235], v[132:133], v[244:245]
	v_pk_fma_f32 v[246:247], v[242:243], v[132:133], v[246:247]
	v_add_f32_e32 v192, v244, v245
	v_add_f32_e32 v193, v246, v247
	s_add_u32 s0, s93, s43
	s_addc_u32 s1, s20, 0
	global_load_dwordx4 v[24:27], v81, s[0:1]
	s_add_u32 s4, s93, s50
	s_addc_u32 s5, s20, 0
	global_load_dwordx4 v[28:31], v81, s[4:5]
	s_waitcnt vmcnt(8)
	v_lshlrev_b32_e32 v76, 16, v68
	v_mul_f32_e32 v186, v186, v76
	v_lshlrev_b32_e32 v77, 16, v69
	v_mul_f32_e32 v187, v187, v77
	v_lshlrev_b32_e32 v76, 16, v70
	v_mul_f32_e32 v188, v188, v76
	v_lshlrev_b32_e32 v77, 16, v71
	v_mul_f32_e32 v189, v189, v77
	v_lshlrev_b32_e32 v76, 16, v72
	v_mul_f32_e32 v190, v190, v76
	v_lshlrev_b32_e32 v77, 16, v73
	v_mul_f32_e32 v191, v191, v77
	v_lshlrev_b32_e32 v76, 16, v74
	v_mul_f32_e32 v192, v192, v76
	v_lshlrev_b32_e32 v77, 16, v75
	v_mul_f32_e32 v193, v193, v77
	s_nop 1
	v_permlane32_swap_b32_e32 v186, v190
	v_permlane32_swap_b32_e32 v187, v191
	v_permlane32_swap_b32_e32 v188, v192
	v_permlane32_swap_b32_e32 v189, v193
	s_nop 0
	v_add_f32_e32 v186, v186, v190
	v_add_f32_e32 v187, v187, v191
	v_add_f32_e32 v188, v188, v192
	v_add_f32_e32 v189, v189, v193
	s_nop 1
	v_permlane16_swap_b32_e32 v186, v188
	v_permlane16_swap_b32_e32 v187, v189
	s_nop 0
	v_add_f32_e32 v186, v186, v188
	v_add_f32_e32 v187, v187, v189
	s_nop 1
	v_add_f32_dpp v248, v186, v186 row_ror:8 row_mask:0xf bank_mask:0x3
	v_add_f32_dpp v248, v187, v187 row_ror:8 row_mask:0xf bank_mask:0xc
	s_nop 1
	v_add_f32_dpp v248, v248, v248 quad_perm:[1,0,3,2] row_mask:0xf bank_mask:0xf
	s_nop 1
	v_add_f32_dpp v248, v248, v248 quad_perm:[2,3,0,1] row_mask:0xf bank_mask:0xf
	s_nop 1
	v_add_f32_dpp v248, v248, v248 row_half_mirror row_mask:0xf bank_mask:0xf
	v_fma_f32 v202, |v248|, s57, 1.0
	v_mul_f32_e32 v204, v248, v248
	v_rcp_f32_e32 v202, v202
	v_mul_f32_e32 v204, 0xbf38aa3b, v204
	v_cmp_gt_f32_e32 vcc, 0, v248
	v_exp_f32_e32 v204, v204
	v_fmamk_f32 v203, v202, 0x3f07dc22, v216
	v_fmaak_f32 v203, v203, v202, 0x3f35f0e3
	v_fmaak_f32 v203, v203, v202, 0xbe11a98e
	v_fmaak_f32 v203, v203, v202, 0x3e027906
	v_mul_f32_e32 v202, v202, v203
	v_mul_f32_e32 v202, v204, v202
	v_mul_f32_e32 v203, v248, v202
	v_fma_f32 v204, -v248, v202, v248
	v_cndmask_b32_e32 v204, v204, v203, vcc
	v_mul_f32_e32 v204, v201, v204
	s_nop 1
	v_readlane_b32 s51, v204, 0
	v_readlane_b32 s64, v204, 8
	v_readlane_b32 s65, v204, 16
	v_readlane_b32 s78, v204, 24
	v_readlane_b32 s79, v204, 32
	v_readlane_b32 s82, v204, 40
	v_readlane_b32 s84, v204, 48
	v_readlane_b32 s10, v204, 56
	s_waitcnt vmcnt(22)
	v_and_b32_e32 v76, 0xffff0000, v68
	v_and_b32_e32 v77, 0xffff0000, v69
	v_mul_f32_e32 v196, s51, v76
	v_mul_f32_e32 v198, s64, v77
	v_cvt_scalef32_pk_f32_fp4 v[228:229], v36, 1.0
	v_cvt_scalef32_pk_f32_fp4 v[230:231], v36, 1.0 op_sel:[1,0,0]
	v_cvt_scalef32_pk_f32_fp4 v[232:233], v36, 1.0 op_sel:[0,1,0]
	v_cvt_scalef32_pk_f32_fp4 v[234:235], v36, 1.0 op_sel:[1,1,0]
	v_pk_fma_f32 v[178:179], v[196:197], v[228:229], v[178:179] op_sel_hi:[0,1,1]
	v_pk_fma_f32 v[184:185], v[196:197], v[230:231], v[184:185] op_sel_hi:[0,1,1]
	v_pk_fma_f32 v[182:183], v[196:197], v[232:233], v[182:183] op_sel_hi:[0,1,1]
	v_pk_fma_f32 v[180:181], v[196:197], v[234:235], v[180:181] op_sel_hi:[0,1,1]
	v_cvt_scalef32_pk_f32_fp4 v[236:237], v40, 1.0
	v_cvt_scalef32_pk_f32_fp4 v[238:239], v40, 1.0 op_sel:[1,0,0]
	v_cvt_scalef32_pk_f32_fp4 v[240:241], v40, 1.0 op_sel:[0,1,0]
	v_cvt_scalef32_pk_f32_fp4 v[242:243], v40, 1.0 op_sel:[1,1,0]
	v_pk_fma_f32 v[178:179], v[198:199], v[236:237], v[178:179] op_sel_hi:[0,1,1]
	v_pk_fma_f32 v[184:185], v[198:199], v[238:239], v[184:185] op_sel_hi:[0,1,1]
	v_pk_fma_f32 v[182:183], v[198:199], v[240:241], v[182:183] op_sel_hi:[0,1,1]
	v_pk_fma_f32 v[180:181], v[198:199], v[242:243], v[180:181] op_sel_hi:[0,1,1]
	v_cvt_scalef32_pk_f32_fp4 v[228:229], v37, 1.0
	v_cvt_scalef32_pk_f32_fp4 v[230:231], v37, 1.0 op_sel:[1,0,0]
	v_cvt_scalef32_pk_f32_fp4 v[232:233], v37, 1.0 op_sel:[0,1,0]
	v_cvt_scalef32_pk_f32_fp4 v[234:235], v37, 1.0 op_sel:[1,1,0]
	v_pk_fma_f32 v[176:177], v[196:197], v[228:229], v[176:177] op_sel_hi:[0,1,1]
	v_pk_fma_f32 v[174:175], v[196:197], v[230:231], v[174:175] op_sel_hi:[0,1,1]
	v_pk_fma_f32 v[160:161], v[196:197], v[232:233], v[160:161] op_sel_hi:[0,1,1]
	v_pk_fma_f32 v[158:159], v[196:197], v[234:235], v[158:159] op_sel_hi:[0,1,1]
	v_cvt_scalef32_pk_f32_fp4 v[236:237], v41, 1.0
	v_cvt_scalef32_pk_f32_fp4 v[238:239], v41, 1.0 op_sel:[1,0,0]
	v_cvt_scalef32_pk_f32_fp4 v[240:241], v41, 1.0 op_sel:[0,1,0]
	v_cvt_scalef32_pk_f32_fp4 v[242:243], v41, 1.0 op_sel:[1,1,0]
	v_pk_fma_f32 v[176:177], v[198:199], v[236:237], v[176:177] op_sel_hi:[0,1,1]
	v_pk_fma_f32 v[174:175], v[198:199], v[238:239], v[174:175] op_sel_hi:[0,1,1]
	v_pk_fma_f32 v[160:161], v[198:199], v[240:241], v[160:161] op_sel_hi:[0,1,1]
	v_pk_fma_f32 v[158:159], v[198:199], v[242:243], v[158:159] op_sel_hi:[0,1,1]
	v_cvt_scalef32_pk_f32_fp4 v[228:229], v38, 1.0
	v_cvt_scalef32_pk_f32_fp4 v[230:231], v38, 1.0 op_sel:[1,0,0]
	v_cvt_scalef32_pk_f32_fp4 v[232:233], v38, 1.0 op_sel:[0,1,0]
	v_cvt_scalef32_pk_f32_fp4 v[234:235], v38, 1.0 op_sel:[1,1,0]
	v_pk_fma_f32 v[156:157], v[196:197], v[228:229], v[156:157] op_sel_hi:[0,1,1]
	v_pk_fma_f32 v[154:155], v[196:197], v[230:231], v[154:155] op_sel_hi:[0,1,1]
	v_pk_fma_f32 v[152:153], v[196:197], v[232:233], v[152:153] op_sel_hi:[0,1,1]
	v_pk_fma_f32 v[150:151], v[196:197], v[234:235], v[150:151] op_sel_hi:[0,1,1]
	v_cvt_scalef32_pk_f32_fp4 v[236:237], v42, 1.0
	v_cvt_scalef32_pk_f32_fp4 v[238:239], v42, 1.0 op_sel:[1,0,0]
	v_cvt_scalef32_pk_f32_fp4 v[240:241], v42, 1.0 op_sel:[0,1,0]
	v_cvt_scalef32_pk_f32_fp4 v[242:243], v42, 1.0 op_sel:[1,1,0]
	v_pk_fma_f32 v[156:157], v[198:199], v[236:237], v[156:157] op_sel_hi:[0,1,1]
	v_pk_fma_f32 v[154:155], v[198:199], v[238:239], v[154:155] op_sel_hi:[0,1,1]
	v_pk_fma_f32 v[152:153], v[198:199], v[240:241], v[152:153] op_sel_hi:[0,1,1]
	v_pk_fma_f32 v[150:151], v[198:199], v[242:243], v[150:151] op_sel_hi:[0,1,1]
	v_cvt_scalef32_pk_f32_fp4 v[228:229], v39, 1.0
	v_cvt_scalef32_pk_f32_fp4 v[230:231], v39, 1.0 op_sel:[1,0,0]
	v_cvt_scalef32_pk_f32_fp4 v[232:233], v39, 1.0 op_sel:[0,1,0]
	v_cvt_scalef32_pk_f32_fp4 v[234:235], v39, 1.0 op_sel:[1,1,0]
	v_pk_fma_f32 v[148:149], v[196:197], v[228:229], v[148:149] op_sel_hi:[0,1,1]
	v_pk_fma_f32 v[146:147], v[196:197], v[230:231], v[146:147] op_sel_hi:[0,1,1]
	v_pk_fma_f32 v[144:145], v[196:197], v[232:233], v[144:145] op_sel_hi:[0,1,1]
	v_pk_fma_f32 v[142:143], v[196:197], v[234:235], v[142:143] op_sel_hi:[0,1,1]
	v_cvt_scalef32_pk_f32_fp4 v[236:237], v43, 1.0
	v_cvt_scalef32_pk_f32_fp4 v[238:239], v43, 1.0 op_sel:[1,0,0]
	v_cvt_scalef32_pk_f32_fp4 v[240:241], v43, 1.0 op_sel:[0,1,0]
	v_cvt_scalef32_pk_f32_fp4 v[242:243], v43, 1.0 op_sel:[1,1,0]
	v_pk_fma_f32 v[148:149], v[198:199], v[236:237], v[148:149] op_sel_hi:[0,1,1]
	v_pk_fma_f32 v[146:147], v[198:199], v[238:239], v[146:147] op_sel_hi:[0,1,1]
	v_pk_fma_f32 v[144:145], v[198:199], v[240:241], v[144:145] op_sel_hi:[0,1,1]
	v_pk_fma_f32 v[142:143], v[198:199], v[242:243], v[142:143] op_sel_hi:[0,1,1]
	s_add_u32 s0, s89, s24
	s_addc_u32 s1, s92, 0
	global_load_dwordx4 v[36:39], v81, s[0:1]
	s_add_u32 s4, s89, s28
	s_addc_u32 s5, s92, 0
	global_load_dwordx4 v[40:43], v81, s[4:5]
	s_lshr_b32 s8, s24, 6
	s_add_u32 s8, s6, s8
	s_addc_u32 s9, s88, 0
	global_load_dword v68, v83, s[8:9]
	s_lshr_b32 s14, s28, 6
	s_add_u32 s14, s6, s14
	s_addc_u32 s15, s88, 0
	global_load_dword v69, v83, s[14:15]
	s_waitcnt vmcnt(22)
	v_and_b32_e32 v76, 0xffff0000, v70
	v_and_b32_e32 v77, 0xffff0000, v71
	v_mul_f32_e32 v196, s65, v76
	v_mul_f32_e32 v198, s78, v77
	v_cvt_scalef32_pk_f32_fp4 v[228:229], v44, 1.0
	v_cvt_scalef32_pk_f32_fp4 v[230:231], v44, 1.0 op_sel:[1,0,0]
	v_cvt_scalef32_pk_f32_fp4 v[232:233], v44, 1.0 op_sel:[0,1,0]
	v_cvt_scalef32_pk_f32_fp4 v[234:235], v44, 1.0 op_sel:[1,1,0]
	v_pk_fma_f32 v[178:179], v[196:197], v[228:229], v[178:179] op_sel_hi:[0,1,1]
	v_pk_fma_f32 v[184:185], v[196:197], v[230:231], v[184:185] op_sel_hi:[0,1,1]
	v_pk_fma_f32 v[182:183], v[196:197], v[232:233], v[182:183] op_sel_hi:[0,1,1]
	v_pk_fma_f32 v[180:181], v[196:197], v[234:235], v[180:181] op_sel_hi:[0,1,1]
	v_cvt_scalef32_pk_f32_fp4 v[236:237], v48, 1.0
	v_cvt_scalef32_pk_f32_fp4 v[238:239], v48, 1.0 op_sel:[1,0,0]
	v_cvt_scalef32_pk_f32_fp4 v[240:241], v48, 1.0 op_sel:[0,1,0]
	v_cvt_scalef32_pk_f32_fp4 v[242:243], v48, 1.0 op_sel:[1,1,0]
	v_pk_fma_f32 v[178:179], v[198:199], v[236:237], v[178:179] op_sel_hi:[0,1,1]
	v_pk_fma_f32 v[184:185], v[198:199], v[238:239], v[184:185] op_sel_hi:[0,1,1]
	v_pk_fma_f32 v[182:183], v[198:199], v[240:241], v[182:183] op_sel_hi:[0,1,1]
	v_pk_fma_f32 v[180:181], v[198:199], v[242:243], v[180:181] op_sel_hi:[0,1,1]
	v_cvt_scalef32_pk_f32_fp4 v[228:229], v45, 1.0
	v_cvt_scalef32_pk_f32_fp4 v[230:231], v45, 1.0 op_sel:[1,0,0]
	v_cvt_scalef32_pk_f32_fp4 v[232:233], v45, 1.0 op_sel:[0,1,0]
	v_cvt_scalef32_pk_f32_fp4 v[234:235], v45, 1.0 op_sel:[1,1,0]
	v_pk_fma_f32 v[176:177], v[196:197], v[228:229], v[176:177] op_sel_hi:[0,1,1]
	v_pk_fma_f32 v[174:175], v[196:197], v[230:231], v[174:175] op_sel_hi:[0,1,1]
	v_pk_fma_f32 v[160:161], v[196:197], v[232:233], v[160:161] op_sel_hi:[0,1,1]
	v_pk_fma_f32 v[158:159], v[196:197], v[234:235], v[158:159] op_sel_hi:[0,1,1]
	v_cvt_scalef32_pk_f32_fp4 v[236:237], v49, 1.0
	v_cvt_scalef32_pk_f32_fp4 v[238:239], v49, 1.0 op_sel:[1,0,0]
	v_cvt_scalef32_pk_f32_fp4 v[240:241], v49, 1.0 op_sel:[0,1,0]
	v_cvt_scalef32_pk_f32_fp4 v[242:243], v49, 1.0 op_sel:[1,1,0]
	v_pk_fma_f32 v[176:177], v[198:199], v[236:237], v[176:177] op_sel_hi:[0,1,1]
	v_pk_fma_f32 v[174:175], v[198:199], v[238:239], v[174:175] op_sel_hi:[0,1,1]
	v_pk_fma_f32 v[160:161], v[198:199], v[240:241], v[160:161] op_sel_hi:[0,1,1]
	v_pk_fma_f32 v[158:159], v[198:199], v[242:243], v[158:159] op_sel_hi:[0,1,1]
	v_cvt_scalef32_pk_f32_fp4 v[228:229], v46, 1.0
	v_cvt_scalef32_pk_f32_fp4 v[230:231], v46, 1.0 op_sel:[1,0,0]
	v_cvt_scalef32_pk_f32_fp4 v[232:233], v46, 1.0 op_sel:[0,1,0]
	v_cvt_scalef32_pk_f32_fp4 v[234:235], v46, 1.0 op_sel:[1,1,0]
	v_pk_fma_f32 v[156:157], v[196:197], v[228:229], v[156:157] op_sel_hi:[0,1,1]
	v_pk_fma_f32 v[154:155], v[196:197], v[230:231], v[154:155] op_sel_hi:[0,1,1]
	v_pk_fma_f32 v[152:153], v[196:197], v[232:233], v[152:153] op_sel_hi:[0,1,1]
	v_pk_fma_f32 v[150:151], v[196:197], v[234:235], v[150:151] op_sel_hi:[0,1,1]
	v_cvt_scalef32_pk_f32_fp4 v[236:237], v50, 1.0
	v_cvt_scalef32_pk_f32_fp4 v[238:239], v50, 1.0 op_sel:[1,0,0]
	v_cvt_scalef32_pk_f32_fp4 v[240:241], v50, 1.0 op_sel:[0,1,0]
	v_cvt_scalef32_pk_f32_fp4 v[242:243], v50, 1.0 op_sel:[1,1,0]
	v_pk_fma_f32 v[156:157], v[198:199], v[236:237], v[156:157] op_sel_hi:[0,1,1]
	v_pk_fma_f32 v[154:155], v[198:199], v[238:239], v[154:155] op_sel_hi:[0,1,1]
	v_pk_fma_f32 v[152:153], v[198:199], v[240:241], v[152:153] op_sel_hi:[0,1,1]
	v_pk_fma_f32 v[150:151], v[198:199], v[242:243], v[150:151] op_sel_hi:[0,1,1]
	v_cvt_scalef32_pk_f32_fp4 v[228:229], v47, 1.0
	v_cvt_scalef32_pk_f32_fp4 v[230:231], v47, 1.0 op_sel:[1,0,0]
	v_cvt_scalef32_pk_f32_fp4 v[232:233], v47, 1.0 op_sel:[0,1,0]
	v_cvt_scalef32_pk_f32_fp4 v[234:235], v47, 1.0 op_sel:[1,1,0]
	v_pk_fma_f32 v[148:149], v[196:197], v[228:229], v[148:149] op_sel_hi:[0,1,1]
	v_pk_fma_f32 v[146:147], v[196:197], v[230:231], v[146:147] op_sel_hi:[0,1,1]
	v_pk_fma_f32 v[144:145], v[196:197], v[232:233], v[144:145] op_sel_hi:[0,1,1]
	v_pk_fma_f32 v[142:143], v[196:197], v[234:235], v[142:143] op_sel_hi:[0,1,1]
	v_cvt_scalef32_pk_f32_fp4 v[236:237], v51, 1.0
	v_cvt_scalef32_pk_f32_fp4 v[238:239], v51, 1.0 op_sel:[1,0,0]
	v_cvt_scalef32_pk_f32_fp4 v[240:241], v51, 1.0 op_sel:[0,1,0]
	v_cvt_scalef32_pk_f32_fp4 v[242:243], v51, 1.0 op_sel:[1,1,0]
	v_pk_fma_f32 v[148:149], v[198:199], v[236:237], v[148:149] op_sel_hi:[0,1,1]
	v_pk_fma_f32 v[146:147], v[198:199], v[238:239], v[146:147] op_sel_hi:[0,1,1]
	v_pk_fma_f32 v[144:145], v[198:199], v[240:241], v[144:145] op_sel_hi:[0,1,1]
	v_pk_fma_f32 v[142:143], v[198:199], v[242:243], v[142:143] op_sel_hi:[0,1,1]
	s_add_u32 s0, s89, s29
	s_addc_u32 s1, s92, 0
	global_load_dwordx4 v[44:47], v81, s[0:1]
	s_add_u32 s4, s89, s34
	s_addc_u32 s5, s92, 0
	global_load_dwordx4 v[48:51], v81, s[4:5]
	s_lshr_b32 s8, s29, 6
	s_add_u32 s8, s6, s8
	s_addc_u32 s9, s88, 0
	global_load_dword v70, v83, s[8:9]
	s_lshr_b32 s14, s34, 6
	s_add_u32 s14, s6, s14
	s_addc_u32 s15, s88, 0
	global_load_dword v71, v83, s[14:15]
	s_waitcnt vmcnt(22)
	v_and_b32_e32 v76, 0xffff0000, v72
	v_and_b32_e32 v77, 0xffff0000, v73
	v_mul_f32_e32 v196, s79, v76
	v_mul_f32_e32 v198, s82, v77
	v_cvt_scalef32_pk_f32_fp4 v[228:229], v52, 1.0
	v_cvt_scalef32_pk_f32_fp4 v[230:231], v52, 1.0 op_sel:[1,0,0]
	v_cvt_scalef32_pk_f32_fp4 v[232:233], v52, 1.0 op_sel:[0,1,0]
	v_cvt_scalef32_pk_f32_fp4 v[234:235], v52, 1.0 op_sel:[1,1,0]
	v_pk_fma_f32 v[178:179], v[196:197], v[228:229], v[178:179] op_sel_hi:[0,1,1]
	v_pk_fma_f32 v[184:185], v[196:197], v[230:231], v[184:185] op_sel_hi:[0,1,1]
	v_pk_fma_f32 v[182:183], v[196:197], v[232:233], v[182:183] op_sel_hi:[0,1,1]
	v_pk_fma_f32 v[180:181], v[196:197], v[234:235], v[180:181] op_sel_hi:[0,1,1]
	v_cvt_scalef32_pk_f32_fp4 v[236:237], v56, 1.0
	v_cvt_scalef32_pk_f32_fp4 v[238:239], v56, 1.0 op_sel:[1,0,0]
	v_cvt_scalef32_pk_f32_fp4 v[240:241], v56, 1.0 op_sel:[0,1,0]
	v_cvt_scalef32_pk_f32_fp4 v[242:243], v56, 1.0 op_sel:[1,1,0]
	v_pk_fma_f32 v[178:179], v[198:199], v[236:237], v[178:179] op_sel_hi:[0,1,1]
	v_pk_fma_f32 v[184:185], v[198:199], v[238:239], v[184:185] op_sel_hi:[0,1,1]
	v_pk_fma_f32 v[182:183], v[198:199], v[240:241], v[182:183] op_sel_hi:[0,1,1]
	v_pk_fma_f32 v[180:181], v[198:199], v[242:243], v[180:181] op_sel_hi:[0,1,1]
	v_cvt_scalef32_pk_f32_fp4 v[228:229], v53, 1.0
	v_cvt_scalef32_pk_f32_fp4 v[230:231], v53, 1.0 op_sel:[1,0,0]
	v_cvt_scalef32_pk_f32_fp4 v[232:233], v53, 1.0 op_sel:[0,1,0]
	v_cvt_scalef32_pk_f32_fp4 v[234:235], v53, 1.0 op_sel:[1,1,0]
	v_pk_fma_f32 v[176:177], v[196:197], v[228:229], v[176:177] op_sel_hi:[0,1,1]
	v_pk_fma_f32 v[174:175], v[196:197], v[230:231], v[174:175] op_sel_hi:[0,1,1]
	v_pk_fma_f32 v[160:161], v[196:197], v[232:233], v[160:161] op_sel_hi:[0,1,1]
	v_pk_fma_f32 v[158:159], v[196:197], v[234:235], v[158:159] op_sel_hi:[0,1,1]
	v_cvt_scalef32_pk_f32_fp4 v[236:237], v57, 1.0
	v_cvt_scalef32_pk_f32_fp4 v[238:239], v57, 1.0 op_sel:[1,0,0]
	v_cvt_scalef32_pk_f32_fp4 v[240:241], v57, 1.0 op_sel:[0,1,0]
	v_cvt_scalef32_pk_f32_fp4 v[242:243], v57, 1.0 op_sel:[1,1,0]
	v_pk_fma_f32 v[176:177], v[198:199], v[236:237], v[176:177] op_sel_hi:[0,1,1]
	v_pk_fma_f32 v[174:175], v[198:199], v[238:239], v[174:175] op_sel_hi:[0,1,1]
	v_pk_fma_f32 v[160:161], v[198:199], v[240:241], v[160:161] op_sel_hi:[0,1,1]
	v_pk_fma_f32 v[158:159], v[198:199], v[242:243], v[158:159] op_sel_hi:[0,1,1]
	v_cvt_scalef32_pk_f32_fp4 v[228:229], v54, 1.0
	v_cvt_scalef32_pk_f32_fp4 v[230:231], v54, 1.0 op_sel:[1,0,0]
	v_cvt_scalef32_pk_f32_fp4 v[232:233], v54, 1.0 op_sel:[0,1,0]
	v_cvt_scalef32_pk_f32_fp4 v[234:235], v54, 1.0 op_sel:[1,1,0]
	v_pk_fma_f32 v[156:157], v[196:197], v[228:229], v[156:157] op_sel_hi:[0,1,1]
	v_pk_fma_f32 v[154:155], v[196:197], v[230:231], v[154:155] op_sel_hi:[0,1,1]
	v_pk_fma_f32 v[152:153], v[196:197], v[232:233], v[152:153] op_sel_hi:[0,1,1]
	v_pk_fma_f32 v[150:151], v[196:197], v[234:235], v[150:151] op_sel_hi:[0,1,1]
	v_cvt_scalef32_pk_f32_fp4 v[236:237], v58, 1.0
	v_cvt_scalef32_pk_f32_fp4 v[238:239], v58, 1.0 op_sel:[1,0,0]
	v_cvt_scalef32_pk_f32_fp4 v[240:241], v58, 1.0 op_sel:[0,1,0]
	v_cvt_scalef32_pk_f32_fp4 v[242:243], v58, 1.0 op_sel:[1,1,0]
	v_pk_fma_f32 v[156:157], v[198:199], v[236:237], v[156:157] op_sel_hi:[0,1,1]
	v_pk_fma_f32 v[154:155], v[198:199], v[238:239], v[154:155] op_sel_hi:[0,1,1]
	v_pk_fma_f32 v[152:153], v[198:199], v[240:241], v[152:153] op_sel_hi:[0,1,1]
	v_pk_fma_f32 v[150:151], v[198:199], v[242:243], v[150:151] op_sel_hi:[0,1,1]
	v_cvt_scalef32_pk_f32_fp4 v[228:229], v55, 1.0
	v_cvt_scalef32_pk_f32_fp4 v[230:231], v55, 1.0 op_sel:[1,0,0]
	v_cvt_scalef32_pk_f32_fp4 v[232:233], v55, 1.0 op_sel:[0,1,0]
	v_cvt_scalef32_pk_f32_fp4 v[234:235], v55, 1.0 op_sel:[1,1,0]
	v_pk_fma_f32 v[148:149], v[196:197], v[228:229], v[148:149] op_sel_hi:[0,1,1]
	v_pk_fma_f32 v[146:147], v[196:197], v[230:231], v[146:147] op_sel_hi:[0,1,1]
	v_pk_fma_f32 v[144:145], v[196:197], v[232:233], v[144:145] op_sel_hi:[0,1,1]
	v_pk_fma_f32 v[142:143], v[196:197], v[234:235], v[142:143] op_sel_hi:[0,1,1]
	v_cvt_scalef32_pk_f32_fp4 v[236:237], v59, 1.0
	v_cvt_scalef32_pk_f32_fp4 v[238:239], v59, 1.0 op_sel:[1,0,0]
	v_cvt_scalef32_pk_f32_fp4 v[240:241], v59, 1.0 op_sel:[0,1,0]
	v_cvt_scalef32_pk_f32_fp4 v[242:243], v59, 1.0 op_sel:[1,1,0]
	v_pk_fma_f32 v[148:149], v[198:199], v[236:237], v[148:149] op_sel_hi:[0,1,1]
	v_pk_fma_f32 v[146:147], v[198:199], v[238:239], v[146:147] op_sel_hi:[0,1,1]
	v_pk_fma_f32 v[144:145], v[198:199], v[240:241], v[144:145] op_sel_hi:[0,1,1]
	v_pk_fma_f32 v[142:143], v[198:199], v[242:243], v[142:143] op_sel_hi:[0,1,1]
	s_add_u32 s0, s89, s35
	s_addc_u32 s1, s92, 0
	global_load_dwordx4 v[52:55], v81, s[0:1]
	s_add_u32 s4, s89, s42
	s_addc_u32 s5, s92, 0
	global_load_dwordx4 v[56:59], v81, s[4:5]
	s_lshr_b32 s8, s35, 6
	s_add_u32 s8, s6, s8
	s_addc_u32 s9, s88, 0
	global_load_dword v72, v83, s[8:9]
	s_lshr_b32 s14, s42, 6
	s_add_u32 s14, s6, s14
	s_addc_u32 s15, s88, 0
	global_load_dword v73, v83, s[14:15]
	s_waitcnt vmcnt(22)
	v_and_b32_e32 v76, 0xffff0000, v74
	v_and_b32_e32 v77, 0xffff0000, v75
	v_mul_f32_e32 v196, s84, v76
	v_mul_f32_e32 v198, s10, v77
	v_cvt_scalef32_pk_f32_fp4 v[228:229], v60, 1.0
	v_cvt_scalef32_pk_f32_fp4 v[230:231], v60, 1.0 op_sel:[1,0,0]
	v_cvt_scalef32_pk_f32_fp4 v[232:233], v60, 1.0 op_sel:[0,1,0]
	v_cvt_scalef32_pk_f32_fp4 v[234:235], v60, 1.0 op_sel:[1,1,0]
	v_pk_fma_f32 v[178:179], v[196:197], v[228:229], v[178:179] op_sel_hi:[0,1,1]
	v_pk_fma_f32 v[184:185], v[196:197], v[230:231], v[184:185] op_sel_hi:[0,1,1]
	v_pk_fma_f32 v[182:183], v[196:197], v[232:233], v[182:183] op_sel_hi:[0,1,1]
	v_pk_fma_f32 v[180:181], v[196:197], v[234:235], v[180:181] op_sel_hi:[0,1,1]
	v_cvt_scalef32_pk_f32_fp4 v[236:237], v64, 1.0
	v_cvt_scalef32_pk_f32_fp4 v[238:239], v64, 1.0 op_sel:[1,0,0]
	v_cvt_scalef32_pk_f32_fp4 v[240:241], v64, 1.0 op_sel:[0,1,0]
	v_cvt_scalef32_pk_f32_fp4 v[242:243], v64, 1.0 op_sel:[1,1,0]
	v_pk_fma_f32 v[178:179], v[198:199], v[236:237], v[178:179] op_sel_hi:[0,1,1]
	v_pk_fma_f32 v[184:185], v[198:199], v[238:239], v[184:185] op_sel_hi:[0,1,1]
	v_pk_fma_f32 v[182:183], v[198:199], v[240:241], v[182:183] op_sel_hi:[0,1,1]
	v_pk_fma_f32 v[180:181], v[198:199], v[242:243], v[180:181] op_sel_hi:[0,1,1]
	v_cvt_scalef32_pk_f32_fp4 v[228:229], v61, 1.0
	v_cvt_scalef32_pk_f32_fp4 v[230:231], v61, 1.0 op_sel:[1,0,0]
	v_cvt_scalef32_pk_f32_fp4 v[232:233], v61, 1.0 op_sel:[0,1,0]
	v_cvt_scalef32_pk_f32_fp4 v[234:235], v61, 1.0 op_sel:[1,1,0]
	v_pk_fma_f32 v[176:177], v[196:197], v[228:229], v[176:177] op_sel_hi:[0,1,1]
	v_pk_fma_f32 v[174:175], v[196:197], v[230:231], v[174:175] op_sel_hi:[0,1,1]
	v_pk_fma_f32 v[160:161], v[196:197], v[232:233], v[160:161] op_sel_hi:[0,1,1]
	v_pk_fma_f32 v[158:159], v[196:197], v[234:235], v[158:159] op_sel_hi:[0,1,1]
	v_cvt_scalef32_pk_f32_fp4 v[236:237], v65, 1.0
	v_cvt_scalef32_pk_f32_fp4 v[238:239], v65, 1.0 op_sel:[1,0,0]
	v_cvt_scalef32_pk_f32_fp4 v[240:241], v65, 1.0 op_sel:[0,1,0]
	v_cvt_scalef32_pk_f32_fp4 v[242:243], v65, 1.0 op_sel:[1,1,0]
	v_pk_fma_f32 v[176:177], v[198:199], v[236:237], v[176:177] op_sel_hi:[0,1,1]
	v_pk_fma_f32 v[174:175], v[198:199], v[238:239], v[174:175] op_sel_hi:[0,1,1]
	v_pk_fma_f32 v[160:161], v[198:199], v[240:241], v[160:161] op_sel_hi:[0,1,1]
	v_pk_fma_f32 v[158:159], v[198:199], v[242:243], v[158:159] op_sel_hi:[0,1,1]
	v_cvt_scalef32_pk_f32_fp4 v[228:229], v62, 1.0
	v_cvt_scalef32_pk_f32_fp4 v[230:231], v62, 1.0 op_sel:[1,0,0]
	v_cvt_scalef32_pk_f32_fp4 v[232:233], v62, 1.0 op_sel:[0,1,0]
	v_cvt_scalef32_pk_f32_fp4 v[234:235], v62, 1.0 op_sel:[1,1,0]
	v_pk_fma_f32 v[156:157], v[196:197], v[228:229], v[156:157] op_sel_hi:[0,1,1]
	v_pk_fma_f32 v[154:155], v[196:197], v[230:231], v[154:155] op_sel_hi:[0,1,1]
	v_pk_fma_f32 v[152:153], v[196:197], v[232:233], v[152:153] op_sel_hi:[0,1,1]
	v_pk_fma_f32 v[150:151], v[196:197], v[234:235], v[150:151] op_sel_hi:[0,1,1]
	v_cvt_scalef32_pk_f32_fp4 v[236:237], v66, 1.0
	v_cvt_scalef32_pk_f32_fp4 v[238:239], v66, 1.0 op_sel:[1,0,0]
	v_cvt_scalef32_pk_f32_fp4 v[240:241], v66, 1.0 op_sel:[0,1,0]
	v_cvt_scalef32_pk_f32_fp4 v[242:243], v66, 1.0 op_sel:[1,1,0]
	v_pk_fma_f32 v[156:157], v[198:199], v[236:237], v[156:157] op_sel_hi:[0,1,1]
	v_pk_fma_f32 v[154:155], v[198:199], v[238:239], v[154:155] op_sel_hi:[0,1,1]
	v_pk_fma_f32 v[152:153], v[198:199], v[240:241], v[152:153] op_sel_hi:[0,1,1]
	v_pk_fma_f32 v[150:151], v[198:199], v[242:243], v[150:151] op_sel_hi:[0,1,1]
	v_cvt_scalef32_pk_f32_fp4 v[228:229], v63, 1.0
	v_cvt_scalef32_pk_f32_fp4 v[230:231], v63, 1.0 op_sel:[1,0,0]
	v_cvt_scalef32_pk_f32_fp4 v[232:233], v63, 1.0 op_sel:[0,1,0]
	v_cvt_scalef32_pk_f32_fp4 v[234:235], v63, 1.0 op_sel:[1,1,0]
	v_pk_fma_f32 v[148:149], v[196:197], v[228:229], v[148:149] op_sel_hi:[0,1,1]
	v_pk_fma_f32 v[146:147], v[196:197], v[230:231], v[146:147] op_sel_hi:[0,1,1]
	v_pk_fma_f32 v[144:145], v[196:197], v[232:233], v[144:145] op_sel_hi:[0,1,1]
	v_pk_fma_f32 v[142:143], v[196:197], v[234:235], v[142:143] op_sel_hi:[0,1,1]
	v_cvt_scalef32_pk_f32_fp4 v[236:237], v67, 1.0
	v_cvt_scalef32_pk_f32_fp4 v[238:239], v67, 1.0 op_sel:[1,0,0]
	v_cvt_scalef32_pk_f32_fp4 v[240:241], v67, 1.0 op_sel:[0,1,0]
	v_cvt_scalef32_pk_f32_fp4 v[242:243], v67, 1.0 op_sel:[1,1,0]
	v_pk_fma_f32 v[148:149], v[198:199], v[236:237], v[148:149] op_sel_hi:[0,1,1]
	v_pk_fma_f32 v[146:147], v[198:199], v[238:239], v[146:147] op_sel_hi:[0,1,1]
	v_pk_fma_f32 v[144:145], v[198:199], v[240:241], v[144:145] op_sel_hi:[0,1,1]
	v_pk_fma_f32 v[142:143], v[198:199], v[242:243], v[142:143] op_sel_hi:[0,1,1]
	s_add_u32 s0, s89, s43
	s_addc_u32 s1, s92, 0
	global_load_dwordx4 v[60:63], v81, s[0:1]
	s_add_u32 s4, s89, s50
	s_addc_u32 s5, s92, 0
	global_load_dwordx4 v[64:67], v81, s[4:5]
	s_lshr_b32 s8, s43, 6
	s_add_u32 s8, s6, s8
	s_addc_u32 s9, s88, 0
	global_load_dword v74, v83, s[8:9]
	s_lshr_b32 s14, s50, 6
	s_add_u32 s14, s6, s14
	s_addc_u32 s15, s88, 0
	global_load_dword v75, v83, s[14:15]
	s_add_i32 s2, s2, 64
	s_cmpk_lt_u32 s2, 0x400
	s_cbranch_scc1 .Lgm_loop
.Lge_epi:
	s_ashr_i32 s2, s44, 13
	s_lshl_b64 s[0:1], s[44:45], 12
	v_lshl_add_u64 v[32:33], v[94:95], 0, s[0:1]
	global_load_dwordx4 v[0:3], v[32:33], off offset:0
	global_load_dwordx4 v[4:7], v[32:33], off offset:16
	global_load_dwordx4 v[8:11], v[32:33], off offset:32
	global_load_dwordx4 v[12:15], v[32:33], off offset:48
	s_waitcnt vmcnt(4)
	v_lshlrev_b32_e32 v34, 4, v80
	v_add_u32_e32 v34, 0x4000, v34
	s_lshl_b32 s10, s2, 13
	v_add_u32_e32 v35, s10, v34
	ds_read_b128 v[36:39], v35 offset:0
	ds_read_b128 v[40:43], v35 offset:1024
	ds_read_b128 v[44:47], v35 offset:2048
	ds_read_b128 v[48:51], v35 offset:3072
	ds_read_b128 v[52:55], v35 offset:4096
	ds_read_b128 v[56:59], v35 offset:5120
	ds_read_b128 v[60:63], v35 offset:6144
	ds_read_b128 v[64:67], v35 offset:7168
	s_lshl_b32 s10, s2, 14
	v_add_u32_e32 v34, s10, v34
	s_waitcnt vmcnt(0) lgkmcnt(0)
	v_lshlrev_b32_e32 v70, 16, v0
	v_and_b32_e32 v71, 0xffff0000, v0
	v_pk_fma_f32 v[100:101], v[178:179], v[36:37], v[70:71]
	v_lshlrev_b32_e32 v70, 16, v1
	v_and_b32_e32 v71, 0xffff0000, v1
	v_pk_fma_f32 v[102:103], v[184:185], v[38:39], v[70:71]
	v_lshlrev_b32_e32 v70, 16, v2
	v_and_b32_e32 v71, 0xffff0000, v2
	v_pk_fma_f32 v[104:105], v[182:183], v[40:41], v[70:71]
	v_lshlrev_b32_e32 v70, 16, v3
	v_and_b32_e32 v71, 0xffff0000, v3
	v_pk_fma_f32 v[106:107], v[180:181], v[42:43], v[70:71]
	v_lshlrev_b32_e32 v70, 16, v4
	v_and_b32_e32 v71, 0xffff0000, v4
	v_pk_fma_f32 v[108:109], v[176:177], v[44:45], v[70:71]
	v_lshlrev_b32_e32 v70, 16, v5
	v_and_b32_e32 v71, 0xffff0000, v5
	v_pk_fma_f32 v[110:111], v[174:175], v[46:47], v[70:71]
	v_lshlrev_b32_e32 v70, 16, v6
	v_and_b32_e32 v71, 0xffff0000, v6
	v_pk_fma_f32 v[112:113], v[160:161], v[48:49], v[70:71]
	v_lshlrev_b32_e32 v70, 16, v7
	v_and_b32_e32 v71, 0xffff0000, v7
	v_pk_fma_f32 v[114:115], v[158:159], v[50:51], v[70:71]
	v_lshlrev_b32_e32 v70, 16, v8
	v_and_b32_e32 v71, 0xffff0000, v8
	v_pk_fma_f32 v[116:117], v[156:157], v[52:53], v[70:71]
	v_lshlrev_b32_e32 v70, 16, v9
	v_and_b32_e32 v71, 0xffff0000, v9
	v_pk_fma_f32 v[118:119], v[154:155], v[54:55], v[70:71]
	v_lshlrev_b32_e32 v70, 16, v10
	v_and_b32_e32 v71, 0xffff0000, v10
	v_pk_fma_f32 v[120:121], v[152:153], v[56:57], v[70:71]
	v_lshlrev_b32_e32 v70, 16, v11
	v_and_b32_e32 v71, 0xffff0000, v11
	v_pk_fma_f32 v[122:123], v[150:151], v[58:59], v[70:71]
	v_lshlrev_b32_e32 v70, 16, v12
	v_and_b32_e32 v71, 0xffff0000, v12
	v_pk_fma_f32 v[124:125], v[148:149], v[60:61], v[70:71]
	v_lshlrev_b32_e32 v70, 16, v13
	v_and_b32_e32 v71, 0xffff0000, v13
	v_pk_fma_f32 v[126:127], v[146:147], v[62:63], v[70:71]
	v_lshlrev_b32_e32 v70, 16, v14
	v_and_b32_e32 v71, 0xffff0000, v14
	v_pk_fma_f32 v[128:129], v[144:145], v[64:65], v[70:71]
	v_lshlrev_b32_e32 v70, 16, v15
	v_and_b32_e32 v71, 0xffff0000, v15
	v_pk_fma_f32 v[130:131], v[142:143], v[66:67], v[70:71]
	v_pk_mul_f32 v[72:73], v[100:101], v[100:101]
	v_pk_fma_f32 v[72:73], v[102:103], v[102:103], v[72:73]
	v_pk_fma_f32 v[72:73], v[104:105], v[104:105], v[72:73]
	v_pk_fma_f32 v[72:73], v[106:107], v[106:107], v[72:73]
	v_pk_fma_f32 v[72:73], v[108:109], v[108:109], v[72:73]
	v_pk_fma_f32 v[72:73], v[110:111], v[110:111], v[72:73]
	v_pk_fma_f32 v[72:73], v[112:113], v[112:113], v[72:73]
	v_pk_fma_f32 v[72:73], v[114:115], v[114:115], v[72:73]
	v_pk_fma_f32 v[72:73], v[116:117], v[116:117], v[72:73]
	v_pk_fma_f32 v[72:73], v[118:119], v[118:119], v[72:73]
	v_pk_fma_f32 v[72:73], v[120:121], v[120:121], v[72:73]
	v_pk_fma_f32 v[72:73], v[122:123], v[122:123], v[72:73]
	v_pk_fma_f32 v[72:73], v[124:125], v[124:125], v[72:73]
	v_pk_fma_f32 v[72:73], v[126:127], v[126:127], v[72:73]
	v_pk_fma_f32 v[72:73], v[128:129], v[128:129], v[72:73]
	v_pk_fma_f32 v[72:73], v[130:131], v[130:131], v[72:73]
	v_add_f32_e32 v72, v72, v73
	s_and_b64 vcc, exec, s[52:53]
	s_cbranch_vccz .Lge_noxc
	v_cvt_pk_bf16_f32 v0, v100, v101
	v_cvt_pk_bf16_f32 v1, v102, v103
	v_cvt_pk_bf16_f32 v2, v104, v105
	v_cvt_pk_bf16_f32 v3, v106, v107
	v_cvt_pk_bf16_f32 v4, v108, v109
	v_cvt_pk_bf16_f32 v5, v110, v111
	v_cvt_pk_bf16_f32 v6, v112, v113
	v_cvt_pk_bf16_f32 v7, v114, v115
	v_cvt_pk_bf16_f32 v8, v116, v117
	v_cvt_pk_bf16_f32 v9, v118, v119
	v_cvt_pk_bf16_f32 v10, v120, v121
	v_cvt_pk_bf16_f32 v11, v122, v123
	v_cvt_pk_bf16_f32 v12, v124, v125
	v_cvt_pk_bf16_f32 v13, v126, v127
	v_cvt_pk_bf16_f32 v14, v128, v129
	v_cvt_pk_bf16_f32 v15, v130, v131
	global_store_dwordx4 v[32:33], v[0:3], off offset:0
	global_store_dwordx4 v[32:33], v[4:7], off offset:16
	global_store_dwordx4 v[32:33], v[8:11], off offset:32
	global_store_dwordx4 v[32:33], v[12:15], off offset:48
